# v62 plus sel-attn selection-mask words requested with the Q fragments before the first unit barrier
# baseline (speedup 1.0000x reference)
; __device__ __forceinline__ unsigned* selp(unsigned char* ws, int t, int g) { return (unsigned*)(ws + WS_PROJ + (size_t)t * (PLD * 2) + 6272 + g * 32); }
;     ...
;         for (int qd = 0; qd < NQ; ++qd) { const bf16_t* qp = proj + (size_t)(tw0 + 4 * qd + (n >> 2)) * PLD + qcol + hr * 64 + 8 * q;
;             Bq[qd][0] = *(const bf16x8*)qp; Bq[qd][1] = *(const bf16x8*)(qp + 32);
;             graw[qd] = (MODE != 0) ? proj[(size_t)(tw0 + 4 * qd + (n >> 2)) * PLD + PC_GL + (MODE == 2 ? 0 : (MODE == 3 ? 8 : 16)) + g * 4 + hr] : (bf16_t)0; }
;         if (MODE == 0) sinkv = inptr(c, I_SINK)[layer * 8 + g * 4 + hr];
;         __syncthreads();
;         if (MODE == 3) {
;             if (c.tid < 8) need[c.tid] = 0u;
;             __syncthreads();
;             { const int tok = c.tid >> 3, w8 = c.tid & 7; const unsigned mw = selp((unsigned char*)sel, t0 + tok, g)[w8]; selm[tok * 8 + w8] = mw; atomicOr((unsigned*)&need[w8], mw); }
.LBB0_1121:
	s_and_b32 s0, s20, 1
	s_lshr_b32 s1, s20, 1
	s_sub_i32 s1, 0xff, s1
	s_lshl_b32 s1, s1, 6
	s_add_i32 s22, s1, s21
	v_or_b32_e32 v196, s22, v155
	s_lshl_b32 s2, s0, 8
	s_lshl_b32 s12, s0, 2
	v_ashrrev_i32_e32 v197, 31, v196
	s_ashr_i32 s3, s2, 31
	s_ashr_i32 s13, s12, 31
	v_lshlrev_b64 v[58:59], 13, v[196:197]
	v_or_b32_e32 v184, 4, v196
	v_lshl_add_u64 v[66:67], s[80:81], 0, v[58:59]
	s_lshl_b64 s[2:3], s[2:3], 1
	s_lshl_b64 s[4:5], s[12:13], 1
	v_ashrrev_i32_e32 v185, 31, v184
	v_lshl_add_u64 v[58:59], v[66:67], 0, s[2:3]
	v_lshl_add_u64 v[66:67], v[66:67], 0, s[4:5]
	v_mov_b32_e32 v165, v1
	v_lshlrev_b64 v[68:69], 13, v[184:185]
	v_lshl_add_u64 v[66:67], v[66:67], 0, v[164:165]
	v_lshl_add_u64 v[70:71], s[80:81], 0, v[68:69]
	v_add_co_u32_e32 v66, vcc, s97, v66
	v_lshl_add_u64 v[68:69], v[70:71], 0, s[2:3]
	v_lshl_add_u64 v[70:71], v[70:71], 0, s[4:5]
	v_lshl_add_u64 v[58:59], v[58:59], 0, v[0:1]
	v_mov_b32_e32 v163, v1
	v_addc_co_u32_e32 v67, vcc, 0, v67, vcc
	v_lshl_add_u64 v[68:69], v[68:69], 0, v[0:1]
	v_lshl_add_u64 v[70:71], v[70:71], 0, v[164:165]
	v_lshl_add_u64 v[62:63], v[58:59], 0, v[162:163]
	v_lshl_add_u64 v[72:73], v[68:69], 0, v[162:163]
	v_add_co_u32_e32 v74, vcc, 0x1000, v70
	global_load_dwordx4 v[58:61], v[62:63], off offset:3584
	s_nop 0
	global_load_dwordx4 v[62:65], v[62:63], off offset:3648
	s_nop 0
	global_load_ushort v235, v[66:67], off offset:2064
	s_nop 0
	global_load_dwordx4 v[66:69], v[72:73], off offset:3584
	v_addc_co_u32_e32 v75, vcc, 0, v71, vcc
	global_load_dwordx4 v[70:73], v[72:73], off offset:3648
	s_nop 0
	global_load_ushort v163, v[74:75], off offset:2064
	s_nop 0
	v_add_u32_e32 v74, s1, v221
	v_ashrrev_i32_e32 v75, 31, v74
	v_lshlrev_b64 v[74:75], 13, v[74:75]
	s_lshl_b32 s2, s0, 5
	v_lshl_add_u64 v[74:75], s[76:77], 0, v[74:75]
	s_ashr_i32 s3, s2, 31
	v_lshl_add_u64 v[74:75], v[74:75], 0, s[2:3]
	v_mov_b32_e32 v167, v1
	v_lshl_add_u64 v[74:75], v[74:75], 0, v[166:167]
	v_add_co_u32_e32 v74, vcc, 0x7f01000, v74
	v_addc_co_u32_e32 v75, vcc, 0, v75, vcc
	global_load_dword v74, v[74:75], off offset:2176
	s_waitcnt lgkmcnt(0)
	s_barrier
	s_and_saveexec_b64 s[2:3], s[38:39]
	ds_write_b32 v225, v1
	s_or_b64 exec, exec, s[2:3]
	s_waitcnt lgkmcnt(0)
	s_nop 0
	s_barrier
	s_waitcnt vmcnt(0)
	ds_write_b32 v222, v74
	ds_or_b32 v223, v74
	s_waitcnt lgkmcnt(0)
	s_barrier
	s_and_saveexec_b64 s[2:3], s[6:7]
	s_cbranch_execz .LBB0_1138
	v_readlane_b32 s1, v253, 33
	v_lshlrev_b32_e64 v75, v154, 1
	s_nop 0
	v_lshl_add_u32 v74, v226, 2, s1
	ds_read_b32 v74, v74
	s_waitcnt lgkmcnt(0)
	v_and_b32_e32 v75, v74, v75
	v_cmp_ne_u32_e32 vcc, 0, v75
	s_and_b64 exec, exec, vcc
	s_cbranch_execz .LBB0_1138
	v_and_b32_e32 v74, v74, v227
	v_bcnt_u32_b32 v74, v74, 0
	s_and_saveexec_b64 s[4:5], s[46:47]
	s_cbranch_execz .LBB0_1137
	s_mov_b64 s[16:17], -1
	v_mov_b32_e32 v75, 0
	s_and_saveexec_b64 s[14:15], s[48:49]
	s_cbranch_execz .LBB0_1132
	v_mov_b32_e32 v75, 0
	s_mov_b64 s[16:17], 0
	v_mov_b32_e32 v76, 0
	v_mov_b32_e32 v77, 0
	v_readlane_b32 s1, v253, 34
	v_mov_b32_e32 v78, v232
